# moe_place: per-block top-4 index load issued with the 16 histogram loads (was alone behind vmcnt(0))
# speedup vs baseline: 1.0003x; 1.0003x over previous
.LBB0_744:
	s_and_saveexec_b64 s[10:11], s[0:1]
	ds_write_b32 v61, v0
	s_or_b64 exec, exec, s[10:11]
	s_waitcnt lgkmcnt(0)
	s_barrier
	global_load_dword v1, v[10:11], off
	global_load_dword v2, v[12:13], off
	global_load_dword v3, v[14:15], off
	global_load_dword v4, v[16:17], off
	global_load_dword v5, v[18:19], off
	global_load_dword v6, v[20:21], off
	global_load_dword v7, v[22:23], off
	global_load_dword v64, v[24:25], off
	global_load_dword v65, v[26:27], off
	global_load_dword v66, v[28:29], off
	global_load_dword v67, v[30:31], off
	global_load_dword v68, v[32:33], off
	global_load_dword v69, v[34:35], off
	global_load_dword v70, v[36:37], off
	global_load_dword v71, v[38:39], off
	global_load_dword v72, v[40:41], off
	v_lshl_add_u32 v200, s90, 8, v8
	v_ashrrev_i32_e32 v201, 31, v200
	v_lshl_add_u64 v[200:201], v[200:201], 2, s[74:75]
	global_load_dword v202, v[200:201], off
	v_cmp_gt_i32_e32 vcc, s90, v44
	s_waitcnt vmcnt(15)
	s_nop 0
	v_cndmask_b32_e32 v73, 0, v1, vcc
	v_cmp_gt_i32_e32 vcc, s90, v45
	s_waitcnt vmcnt(14)
	v_add_u32_e32 v1, v2, v1
	s_waitcnt vmcnt(12)
	v_add3_u32 v1, v1, v3, v4
	v_cndmask_b32_e32 v2, 0, v2, vcc
	v_cmp_gt_i32_e32 vcc, s90, v46
	v_add_u32_e32 v2, v2, v73
	s_waitcnt vmcnt(10)
	v_add3_u32 v1, v1, v5, v6
	v_cndmask_b32_e32 v74, 0, v3, vcc
	v_cmp_gt_i32_e32 vcc, s90, v47
	s_waitcnt vmcnt(8)
	v_add3_u32 v1, v1, v7, v64
	s_waitcnt vmcnt(6)
	v_add3_u32 v1, v1, v65, v66
	v_cndmask_b32_e32 v75, 0, v4, vcc
	v_cmp_gt_i32_e32 vcc, s90, v48
	v_add3_u32 v2, v2, v74, v75
	s_waitcnt vmcnt(4)
	v_add3_u32 v1, v1, v67, v68
	v_cndmask_b32_e32 v76, 0, v5, vcc
	v_cmp_gt_i32_e32 vcc, s90, v49
	s_waitcnt vmcnt(2)
	v_add3_u32 v1, v1, v69, v70
	s_waitcnt vmcnt(0)
	v_add3_u32 v1, v1, v71, v72
	v_cndmask_b32_e32 v77, 0, v6, vcc
	v_cmp_gt_i32_e32 vcc, s90, v50
	v_add3_u32 v2, v2, v76, v77
	v_lshl_add_u32 v6, s90, 8, v8
	v_cndmask_b32_e32 v78, 0, v7, vcc
	v_cmp_gt_i32_e32 vcc, s90, v51
	s_nop 1
	v_cndmask_b32_e32 v79, 0, v64, vcc
	v_cmp_gt_i32_e32 vcc, s90, v52
	v_add3_u32 v2, v2, v78, v79
	s_nop 0
	v_cndmask_b32_e32 v80, 0, v65, vcc
	v_cmp_gt_i32_e32 vcc, s90, v53
	s_nop 1
	v_cndmask_b32_e32 v81, 0, v66, vcc
	v_cmp_gt_i32_e32 vcc, s90, v54
	v_add3_u32 v2, v2, v80, v81
	s_nop 0
	v_cndmask_b32_e32 v82, 0, v67, vcc
	v_cmp_gt_i32_e32 vcc, s90, v55
	s_nop 1
	v_cndmask_b32_e32 v83, 0, v68, vcc
	v_cmp_gt_i32_e32 vcc, s90, v56
	v_add3_u32 v2, v2, v82, v83
	s_nop 0
	v_cndmask_b32_e32 v84, 0, v69, vcc
	v_cmp_gt_i32_e32 vcc, s90, v57
	s_nop 1
	v_cndmask_b32_e32 v85, 0, v70, vcc
	v_cmp_gt_i32_e32 vcc, s90, v58
	v_add3_u32 v2, v2, v84, v85
	s_nop 0
	v_cndmask_b32_e32 v86, 0, v71, vcc
	v_cmp_gt_i32_e32 vcc, s90, v59
	s_nop 1
	v_cndmask_b32_e32 v87, 0, v72, vcc
	v_add3_u32 v2, v2, v86, v87
	ds_add_u32 v60, v1
	ds_add_u32 v60, v2 offset:128
	s_and_saveexec_b64 s[10:11], s[2:3]
	s_cbranch_execz .LBB0_748
	v_ashrrev_i32_e32 v7, 31, v6
	v_lshl_add_u64 v[2:3], v[6:7], 2, s[74:75]
	v_mov_b32_e32 v1, v202
	s_waitcnt vmcnt(0)
	ds_write_b32 v61, v1 offset:384
